# baseline (speedup 1.0000x reference)
.LBB3_6:
	v_mov_b32_e32 v189, v178
	s_lshl_b32 s74, s2, 5
	s_add_i32 s22, s74, s86
	v_mov_b32_e32 v0, v236
	s_add_i32 s0, s2, 0x200
	s_cmpk_gt_i32 s0, 0x61a
	s_cbranch_scc1 .Lk4_nopf
	s_lshl_b32 s0, s0, 5
	s_add_i32 s0, s0, s86
	v_min_i32_e32 v1, 8, v189
	v_add_u32_e32 v1, s0, v1
	v_min_i32_e32 v1, 0xc350, v1
	v_lshlrev_b32_e32 v1, 2, v1
	global_load_dword v236, v1, s[56:57]

.LBB3_141:
	s_or_b64 exec, exec, s[70:71]
	v_max_f32_e32 v170, 0xff7fffff, v170
	v_mul_f32_e32 v243, 0xbfb8aa3b, v170
	s_mov_b32 s32, 0x3fb8aa3b
	v_fma_f32 v163, v173, s32, v243
	v_exp_f32_e32 v224, v163
	v_fma_f32 v164, v175, s32, v243
	v_exp_f32_e32 v222, v164
	v_fma_f32 v163, v174, s32, v243
	v_exp_f32_e32 v223, v163
	v_fma_f32 v164, v195, s32, v243
	v_fma_f32 v163, v176, s32, v243
	v_exp_f32_e32 v221, v163
	v_exp_f32_e32 v220, v164
	v_fma_f32 v161, v172, s32, v243
	v_fma_f32 v163, v196, s32, v243
	v_fma_f32 v164, v197, s32, v243
	v_exp_f32_e32 v219, v163
	v_exp_f32_e32 v218, v164
	v_exp_f32_e32 v225, v161
	v_fma_f32 v163, v198, s32, v243
	v_fma_f32 v164, v199, s32, v243
	v_exp_f32_e32 v217, v163
	v_exp_f32_e32 v216, v164
	v_fma_f32 v163, v200, s32, v243
	v_fma_f32 v164, v201, s32, v243
	v_exp_f32_e32 v215, v163
	v_exp_f32_e32 v214, v164
	v_add_f32_e32 v161, 0, v225
	v_fma_f32 v163, v202, s32, v243
	v_fma_f32 v164, v203, s32, v243
	v_exp_f32_e32 v200, v163
	v_exp_f32_e32 v199, v164
	v_add_f32_e32 v161, v161, v224
	v_fma_f32 v163, v204, s32, v243
	v_fma_f32 v164, v205, s32, v243
	v_exp_f32_e32 v198, v163
	v_exp_f32_e32 v196, v164
	v_add_f32_e32 v161, v161, v223
	v_fma_f32 v163, v206, s32, v243
	v_fma_f32 v164, v207, s32, v243
	v_exp_f32_e32 v195, v163
	v_exp_f32_e32 v176, v164
	v_add_f32_e32 v161, v161, v222
	v_fma_f32 v163, v208, s32, v243
	v_add_f32_e32 v161, v161, v221
	v_fma_f32 v164, v209, s32, v243
	v_add_f32_e32 v161, v161, v220
	v_exp_f32_e32 v175, v163
	v_add_f32_e32 v161, v161, v219
	v_exp_f32_e32 v174, v164
	v_add_f32_e32 v161, v161, v218
	v_add_f32_e32 v161, v161, v217
	v_add_f32_e32 v161, v161, v216
	v_fma_f32 v163, v210, s32, v243
	v_add_f32_e32 v161, v161, v215
	v_fma_f32 v164, v211, s32, v243
	v_add_f32_e32 v161, v161, v214
	v_exp_f32_e32 v173, v163
	v_add_f32_e32 v161, v161, v200
	v_exp_f32_e32 v172, v164
	v_add_f32_e32 v161, v161, v199
	v_add_f32_e32 v161, v161, v198
	v_add_f32_e32 v161, v161, v196
	v_fma_f32 v163, v212, s32, v243
	v_add_f32_e32 v161, v161, v195
	v_fma_f32 v164, v213, s32, v243
	v_add_f32_e32 v161, v161, v176
	v_exp_f32_e32 v163, v163
	v_add_f32_e32 v161, v161, v175
	v_exp_f32_e32 v171, v164
	v_add_f32_e32 v161, v161, v174
	v_add_f32_e32 v161, v161, v173
	v_add_f32_e32 v161, v161, v172
	v_cndmask_b32_e64 v164, 0, v163, s[4:5]
	v_add_f32_e32 v163, v161, v164
	v_cndmask_b32_e64 v161, 0, v171, s[52:53]
	v_add_f32_e32 v163, v163, v161
	s_and_saveexec_b64 s[54:55], s[0:1]
	s_cbranch_execz .LBB3_145
	v_lshlrev_b32_e32 v171, 2, v193
	v_lshl_or_b32 v171, v160, 5, v171
	s_lshl_b32 s69, s78, 5
	v_subrev_u32_e32 v171, s69, v171
	v_add_u32_e32 v171, s93, v171
	s_mov_b32 s69, 24
	s_mov_b64 s[70:71], 0

.LBB3_145:
	s_or_b64 exec, exec, s[54:55]
	v_rcp_f32_e32 v171, v163
	s_movk_i32 s69, 0x410
	v_lshlrev_b32_e32 v197, 6, v189
	v_fma_f32 v202, -v163, v171, 1.0
	v_fmac_f32_e32 v171, v202, v171
	v_cmp_lt_f32_e32 vcc, 0, v163
	v_mul_lo_u32 v169, v169, s69
	v_and_b32_e32 v197, 0x3c0, v197
	v_cndmask_b32_e32 v163, 0, v171, vcc
	v_sub_u32_e32 v171, v160, v168
	v_add3_u32 v201, s99, v169, v197
	s_max_i32 s32, s33, s96
	s_max_i32 s32, s32, s97
	s_max_i32 s32, s32, s75
	s_cmp_gt_i32 s32, 32
	s_cbranch_scc1 .Lk4_slowst
	s_and_saveexec_b64 s[54:55], s[44:45]
	v_lshl_add_u32 v238, v171, 1, v201
	v_fma_mixlo_f16 v239, v163, v225, 0
	ds_write_b16 v238, v239
	v_fma_mixlo_f16 v240, v163, v224, 0
	ds_write_b16 v238, v240 offset:2
	v_fma_mixlo_f16 v241, v163, v223, 0
	ds_write_b16 v238, v241 offset:4
	v_fma_mixlo_f16 v242, v163, v222, 0
	ds_write_b16 v238, v242 offset:6
	v_fma_mixlo_f16 v239, v163, v221, 0
	ds_write_b16 v238, v239 offset:8
	v_fma_mixlo_f16 v240, v163, v220, 0
	ds_write_b16 v238, v240 offset:10
	v_fma_mixlo_f16 v241, v163, v219, 0
	ds_write_b16 v238, v241 offset:12
	v_fma_mixlo_f16 v242, v163, v218, 0
	ds_write_b16 v238, v242 offset:14
	s_cmp_eq_u64 s[34:35], 0
	s_cbranch_scc1 .Lk4_stdone
	v_fma_mixlo_f16 v239, v163, v217, 0
	ds_write_b16 v238, v239 offset:16
	v_fma_mixlo_f16 v240, v163, v216, 0
	ds_write_b16 v238, v240 offset:18
	v_fma_mixlo_f16 v241, v163, v215, 0
	ds_write_b16 v238, v241 offset:20
	v_fma_mixlo_f16 v242, v163, v214, 0
	ds_write_b16 v238, v242 offset:22
	s_cmp_eq_u64 s[24:25], 0
	s_cbranch_scc1 .Lk4_stdone
	v_fma_mixlo_f16 v239, v163, v200, 0
	ds_write_b16 v238, v239 offset:24
	v_fma_mixlo_f16 v240, v163, v199, 0
	ds_write_b16 v238, v240 offset:26
	v_fma_mixlo_f16 v241, v163, v198, 0
	ds_write_b16 v238, v241 offset:28
	v_fma_mixlo_f16 v242, v163, v196, 0
	ds_write_b16 v238, v242 offset:30
	s_cmp_eq_u64 s[16:17], 0
	s_cbranch_scc1 .Lk4_stdone
	v_fma_mixlo_f16 v239, v163, v195, 0
	ds_write_b16 v238, v239 offset:32
	v_fma_mixlo_f16 v240, v163, v176, 0
	ds_write_b16 v238, v240 offset:34
	v_fma_mixlo_f16 v241, v163, v175, 0
	ds_write_b16 v238, v241 offset:36
	v_fma_mixlo_f16 v242, v163, v174, 0
	ds_write_b16 v238, v242 offset:38
	s_cmp_eq_u64 s[8:9], 0
	s_cbranch_scc1 .Lk4_stdone
	v_fma_mixlo_f16 v239, v163, v173, 0
	ds_write_b16 v238, v239 offset:40
	v_fma_mixlo_f16 v240, v163, v172, 0
	ds_write_b16 v238, v240 offset:42
	v_fma_mixlo_f16 v241, v163, v164, 0
	ds_write_b16 v238, v241 offset:44
	v_fma_mixlo_f16 v242, v163, v161, 0
	ds_write_b16 v238, v242 offset:46

	.amdhsa_kernel _Z8k_layer1PKiS0_PKfS2_PK15HIP_vector_typeIjLj4EEPKDv8_DF16_S9_S2_S2_S2_PDF16_PfSB_
		.amdhsa_group_segment_fixed_size 55232
		.amdhsa_private_segment_fixed_size 0
		.amdhsa_kernarg_size 360
		.amdhsa_user_sgpr_count 2
		.amdhsa_user_sgpr_dispatch_ptr 0
		.amdhsa_user_sgpr_queue_ptr 0
		.amdhsa_user_sgpr_kernarg_segment_ptr 1
		.amdhsa_user_sgpr_dispatch_id 0
		.amdhsa_user_sgpr_kernarg_preload_length 0
		.amdhsa_user_sgpr_kernarg_preload_offset 0
		.amdhsa_user_sgpr_private_segment_size 0
		.amdhsa_uses_dynamic_stack 0
		.amdhsa_enable_private_segment 0
		.amdhsa_system_sgpr_workgroup_id_x 1
		.amdhsa_system_sgpr_workgroup_id_y 0
		.amdhsa_system_sgpr_workgroup_id_z 0
		.amdhsa_system_sgpr_workgroup_info 0
		.amdhsa_system_vgpr_workitem_id 0
		.amdhsa_next_free_vgpr 244
		.amdhsa_next_free_sgpr 100
		.amdhsa_accum_offset 244
		.amdhsa_reserve_vcc 1
		.amdhsa_float_round_mode_32 0
		.amdhsa_float_round_mode_16_64 0
		.amdhsa_float_denorm_mode_32 3
		.amdhsa_float_denorm_mode_16_64 3
		.amdhsa_dx10_clamp 1
		.amdhsa_ieee_mode 1
		.amdhsa_fp16_overflow 0
		.amdhsa_tg_split 0
		.amdhsa_exception_fp_ieee_invalid_op 0
		.amdhsa_exception_fp_denorm_src 0
		.amdhsa_exception_fp_ieee_div_zero 0
		.amdhsa_exception_fp_ieee_overflow 0
		.amdhsa_exception_fp_ieee_underflow 0
		.amdhsa_exception_fp_ieee_inexact 0
		.amdhsa_exception_int_div_zero 0
	.end_amdhsa_kernel

amdhsa.kernels:
  - .agpr_count:     0
    .args:
      - .actual_access:  read_only
        .address_space:  global
        .offset:         0
        .size:           8
        .value_kind:     global_buffer
      - .actual_access:  read_only
        .address_space:  global
        .offset:         8
        .size:           8
        .value_kind:     global_buffer
      - .actual_access:  read_only
        .address_space:  global
        .offset:         16
        .size:           8
        .value_kind:     global_buffer
      - .actual_access:  read_only
        .address_space:  global
        .offset:         24
        .size:           8
        .value_kind:     global_buffer
      - .actual_access:  read_only
        .address_space:  global
        .offset:         32
        .size:           8
        .value_kind:     global_buffer
      - .actual_access:  write_only
        .address_space:  global
        .offset:         40
        .size:           8
        .value_kind:     global_buffer
      - .actual_access:  write_only
        .address_space:  global
        .offset:         48
        .size:           8
        .value_kind:     global_buffer
      - .actual_access:  write_only
        .address_space:  global
        .offset:         56
        .size:           8
        .value_kind:     global_buffer
      - .actual_access:  write_only
        .address_space:  global
        .offset:         64
        .size:           8
        .value_kind:     global_buffer
    .group_segment_fixed_size: 1024
    .kernarg_segment_align: 8
    .kernarg_segment_size: 72
    .language:       OpenCL C
    .language_version:
      - 2
      - 0
    .max_flat_workgroup_size: 512
    .name:           _Z11k_hist_prepPKiPKfS2_S2_S2_PiPfPDF16_S5_
    .private_segment_fixed_size: 0
    .sgpr_count:     20
    .sgpr_spill_count: 0
    .symbol:         _Z11k_hist_prepPKiPKfS2_S2_S2_PiPfPDF16_S5_.kd
    .uniform_work_group_size: 1
    .uses_dynamic_stack: false
    .vgpr_count:     42
    .vgpr_spill_count: 0
    .wavefront_size: 64
  - .agpr_count:     0
    .args:
      - .actual_access:  read_only
        .address_space:  global
        .offset:         0
        .size:           8
        .value_kind:     global_buffer
      - .actual_access:  read_only
        .address_space:  global
        .offset:         8
        .size:           8
        .value_kind:     global_buffer
      - .actual_access:  write_only
        .address_space:  global
        .offset:         16
        .size:           8
        .value_kind:     global_buffer
      - .actual_access:  write_only
        .address_space:  global
        .offset:         24
        .size:           8
        .value_kind:     global_buffer
      - .actual_access:  read_only
        .address_space:  global
        .offset:         32
        .size:           8
        .value_kind:     global_buffer
      - .actual_access:  read_only
        .address_space:  global
        .offset:         40
        .size:           8
        .value_kind:     global_buffer
      - .actual_access:  write_only
        .address_space:  global
        .offset:         48
        .size:           8
        .value_kind:     global_buffer
      - .actual_access:  write_only
        .address_space:  global
        .offset:         56
        .size:           8
        .value_kind:     global_buffer
      - .actual_access:  write_only
        .address_space:  global
        .offset:         64
        .size:           8
        .value_kind:     global_buffer
    .group_segment_fixed_size: 9344
    .kernarg_segment_align: 8
    .kernarg_segment_size: 72
    .language:       OpenCL C
    .language_version:
      - 2
      - 0
    .max_flat_workgroup_size: 512
    .name:           _Z14k_scatter_nodePKiS0_PjPiPKfS4_PfS5_PDF16_
    .private_segment_fixed_size: 0
    .sgpr_count:     106
    .sgpr_spill_count: 10
    .symbol:         _Z14k_scatter_nodePKiS0_PjPiPKfS4_PfS5_PDF16_.kd
    .uniform_work_group_size: 1
    .uses_dynamic_stack: false
    .vgpr_count:     118
    .vgpr_spill_count: 0
    .wavefront_size: 64
  - .agpr_count:     0
    .args:
      - .actual_access:  read_only
        .address_space:  global
        .offset:         0
        .size:           8
        .value_kind:     global_buffer
      - .actual_access:  read_only
        .address_space:  global
        .offset:         8
        .size:           8
        .value_kind:     global_buffer
      - .actual_access:  write_only
        .address_space:  global
        .offset:         16
        .size:           8
        .value_kind:     global_buffer
      - .actual_access:  write_only
        .address_space:  global
        .offset:         24
        .size:           8
        .value_kind:     global_buffer
    .group_segment_fixed_size: 3072
    .kernarg_segment_align: 8
    .kernarg_segment_size: 32
    .language:       OpenCL C
    .language_version:
      - 2
      - 0
    .max_flat_workgroup_size: 1024
    .name:           _Z5k_csrPKjPKiPiS3_
    .private_segment_fixed_size: 0
    .sgpr_count:     34
    .sgpr_spill_count: 0
    .symbol:         _Z5k_csrPKjPKiPiS3_.kd
    .uniform_work_group_size: 1
    .uses_dynamic_stack: false
    .vgpr_count:     18
    .vgpr_spill_count: 0
    .wavefront_size: 64
  - .agpr_count:     0
    .args:
      - .actual_access:  read_only
        .address_space:  global
        .offset:         0
        .size:           8
        .value_kind:     global_buffer
      - .actual_access:  read_only
        .address_space:  global
        .offset:         8
        .size:           8
        .value_kind:     global_buffer
      - .actual_access:  read_only
        .address_space:  global
        .offset:         16
        .size:           8
        .value_kind:     global_buffer
      - .actual_access:  read_only
        .address_space:  global
        .offset:         24
        .size:           8
        .value_kind:     global_buffer
      - .actual_access:  read_only
        .address_space:  global
        .offset:         32
        .size:           8
        .value_kind:     global_buffer
      - .actual_access:  read_only
        .address_space:  global
        .offset:         40
        .size:           8
        .value_kind:     global_buffer
      - .actual_access:  read_only
        .address_space:  global
        .offset:         48
        .size:           8
        .value_kind:     global_buffer
      - .actual_access:  read_only
        .address_space:  global
        .offset:         56
        .size:           8
        .value_kind:     global_buffer
      - .actual_access:  read_only
        .address_space:  global
        .offset:         64
        .size:           8
        .value_kind:     global_buffer
      - .actual_access:  read_only
        .address_space:  global
        .offset:         72
        .size:           8
        .value_kind:     global_buffer
      - .actual_access:  write_only
        .address_space:  global
        .offset:         80
        .size:           8
        .value_kind:     global_buffer
      - .actual_access:  write_only
        .address_space:  global
        .offset:         88
        .size:           8
        .value_kind:     global_buffer
      - .actual_access:  write_only
        .address_space:  global
        .offset:         96
        .size:           8
        .value_kind:     global_buffer
      - .offset:         104
        .size:           4
        .value_kind:     hidden_block_count_x
      - .offset:         108
        .size:           4
        .value_kind:     hidden_block_count_y
      - .offset:         112
        .size:           4
        .value_kind:     hidden_block_count_z
      - .offset:         116
        .size:           2
        .value_kind:     hidden_group_size_x
      - .offset:         118
        .size:           2
        .value_kind:     hidden_group_size_y
      - .offset:         120
        .size:           2
        .value_kind:     hidden_group_size_z
      - .offset:         122
        .size:           2
        .value_kind:     hidden_remainder_x
      - .offset:         124
        .size:           2
        .value_kind:     hidden_remainder_y
      - .offset:         126
        .size:           2
        .value_kind:     hidden_remainder_z
      - .offset:         144
        .size:           8
        .value_kind:     hidden_global_offset_x
      - .offset:         152
        .size:           8
        .value_kind:     hidden_global_offset_y
      - .offset:         160
        .size:           8
        .value_kind:     hidden_global_offset_z
      - .offset:         168
        .size:           2
        .value_kind:     hidden_grid_dims
    .group_segment_fixed_size: 55232
    .kernarg_segment_align: 8
    .kernarg_segment_size: 360
    .language:       OpenCL C
    .language_version:
      - 2
      - 0
    .max_flat_workgroup_size: 256
    .name:           _Z8k_layer1PKiS0_PKfS2_PK15HIP_vector_typeIjLj4EEPKDv8_DF16_S9_S2_S2_S2_PDF16_PfSB_
    .private_segment_fixed_size: 0
    .sgpr_count:     106
    .sgpr_spill_count: 7
    .symbol:         _Z8k_layer1PKiS0_PKfS2_PK15HIP_vector_typeIjLj4EEPKDv8_DF16_S9_S2_S2_S2_PDF16_PfSB_.kd
    .uniform_work_group_size: 1
    .uses_dynamic_stack: false
    .vgpr_count:     244
    .vgpr_spill_count: 0
    .wavefront_size: 64
  - .agpr_count:     0
    .args:
      - .actual_access:  read_only
        .address_space:  global
        .offset:         0
        .size:           8
        .value_kind:     global_buffer
      - .actual_access:  read_only
        .address_space:  global
        .offset:         8
        .size:           8
        .value_kind:     global_buffer
      - .actual_access:  read_only
        .address_space:  global
        .offset:         16
        .size:           8
        .value_kind:     global_buffer
      - .actual_access:  read_only
        .address_space:  global
        .offset:         24
        .size:           8
        .value_kind:     global_buffer
      - .actual_access:  read_only
        .address_space:  global
        .offset:         32
        .size:           8
        .value_kind:     global_buffer
      - .actual_access:  read_only
        .address_space:  global
        .offset:         40
        .size:           8
        .value_kind:     global_buffer
      - .actual_access:  write_only
        .address_space:  global
        .offset:         48
        .size:           8
        .value_kind:     global_buffer
    .group_segment_fixed_size: 0
    .kernarg_segment_align: 8
    .kernarg_segment_size: 56
    .language:       OpenCL C
    .language_version:
      - 2
      - 0
    .max_flat_workgroup_size: 256
    .name:           _Z8k_layer2PKiS0_PKfS2_PK15HIP_vector_typeIjLj4EES2_Pf
    .private_segment_fixed_size: 0
    .sgpr_count:     52
    .sgpr_spill_count: 0
    .symbol:         _Z8k_layer2PKiS0_PKfS2_PK15HIP_vector_typeIjLj4EES2_Pf.kd
    .uniform_work_group_size: 1
    .uses_dynamic_stack: false
    .vgpr_count:     70
    .vgpr_spill_count: 0
    .wavefront_size: 64
